# static s_setprio 1 for waves 4-7 during the indexer pass (reset at its end); on top of v65
# speedup vs baseline: 1.0120x; 1.0062x over previous
.LBB0_706:
	s_or_b64 exec, exec, s[0:1]
	s_lshl_b32 s2, s16, 2
	s_andn2_b32 s2, s2, 31
	s_and_b32 s0, s16, 7
	s_and_b32 s1, s13, 1
	s_xor_b32 s6, s2, 0x3e0
	s_cmp_eq_u32 s1, 0
	s_cselect_b32 s1, s2, s6
	s_sub_i32 s6, 0x1fe0, s1
	s_lshl_b32 s25, s0, 13
	s_add_i32 s8, s6, s25
	s_lshl_b32 s2, s0, 20
	s_ashr_i32 s9, s8, 31
	s_ashr_i32 s7, s6, 5
	v_readlane_b32 s0, v254, 49
	s_add_u32 s0, s0, s2
	v_readlane_b32 s1, v254, 50
	s_addc_u32 s1, s1, 0
	s_lshl_b64 s[10:11], s[8:9], 5
	v_lshl_add_u64 v[2:3], v[146:147], 0, s[10:11]
	global_load_dwordx4 v[66:69], v[2:3], off
	global_load_dwordx4 v[70:73], v[2:3], off offset:16
	s_lshl_b64 s[8:9], s[8:9], 10
	v_lshl_add_u64 v[62:63], v[144:145], 0, s[8:9]
	global_load_dwordx4 v[2:5], v[62:63], off
	global_load_dwordx4 v[6:9], v[62:63], off offset:128
	global_load_dwordx4 v[10:13], v[62:63], off offset:256
	global_load_dwordx4 v[14:17], v[62:63], off offset:384
	global_load_dwordx4 v[18:21], v[62:63], off offset:512
	global_load_dwordx4 v[22:25], v[62:63], off offset:640
	global_load_dwordx4 v[26:29], v[62:63], off offset:768
	global_load_dwordx4 v[30:33], v[62:63], off offset:896
	global_load_dwordx4 v[34:37], v[62:63], off offset:64
	global_load_dwordx4 v[38:41], v[62:63], off offset:192
	global_load_dwordx4 v[42:45], v[62:63], off offset:320
	global_load_dwordx4 v[46:49], v[62:63], off offset:448
	global_load_dwordx4 v[50:53], v[62:63], off offset:576
	global_load_dwordx4 v[54:57], v[62:63], off offset:704
	global_load_dwordx4 v[58:61], v[62:63], off offset:832
	s_nop 0
	global_load_dwordx4 v[62:65], v[62:63], off offset:960
	v_lshl_add_u64 v[184:185], s[0:1], 0, v[152:153]
	v_lshl_add_u64 v[184:185], v[184:185], 0, v[154:155]
	s_mov_b64 s[10:11], 0x800
	v_lshl_add_u64 v[186:187], v[184:185], 0, s[10:11]
	global_load_dwordx4 v[134:137], v[184:185], off
	global_load_dwordx4 v[130:133], v[184:185], off offset:1024
	s_mov_b64 s[10:11], 0x1000
	v_lshl_add_u64 v[188:189], v[184:185], 0, s[10:11]
	global_load_dwordx4 v[126:129], v[186:187], off
	global_load_dwordx4 v[122:125], v[186:187], off offset:1024
	s_mov_b64 s[10:11], 0x1800
	v_lshl_add_u64 v[184:185], v[184:185], 0, s[10:11]
	global_load_dwordx4 v[110:113], v[188:189], off
	global_load_dwordx4 v[106:109], v[188:189], off offset:1024
	global_load_dwordx4 v[94:97], v[184:185], off
	global_load_dwordx4 v[90:93], v[184:185], off offset:1024
	s_add_i32 s7, s7, 1
	s_ashr_i32 s9, s6, 4
	s_lshl_b32 s8, s7, 1
	v_lshl_add_u64 v[172:173], s[0:1], 0, v[154:155]
	s_waitcnt lgkmcnt(0)
	s_barrier
	s_waitcnt vmcnt(23)
	v_and_b32_e32 v83, 0xffff0000, v3
	v_lshlrev_b32_e32 v82, 16, v3
	s_waitcnt vmcnt(22)
	v_and_b32_e32 v85, 0xffff0000, v7
	v_mul_f32_e32 v156, 0.5, v66
	v_mul_f32_e32 v158, 0.5, v67
	v_and_b32_e32 v67, 0xffff0000, v2
	v_lshlrev_b32_e32 v66, 16, v2
	v_mul_f32_e32 v160, 0.5, v68
	v_mul_f32_e32 v162, 0.5, v69
	v_and_b32_e32 v69, 0xffff0000, v6
	v_lshlrev_b32_e32 v68, 16, v6
	v_lshlrev_b32_e32 v84, 16, v7
	v_pk_fma_f32 v[66:67], v[156:157], v[66:67], 0 op_sel_hi:[0,1,0]
	v_pk_fma_f32 v[82:83], v[156:157], v[82:83], 0 op_sel_hi:[0,1,0]
	v_mul_f32_e32 v164, 0.5, v70
	v_mul_f32_e32 v166, 0.5, v71
	s_waitcnt vmcnt(21)
	v_and_b32_e32 v71, 0xffff0000, v10
	v_lshlrev_b32_e32 v70, 16, v10
	v_and_b32_e32 v87, 0xffff0000, v11
	v_lshlrev_b32_e32 v86, 16, v11
	v_pk_fma_f32 v[66:67], v[158:159], v[68:69], v[66:67] op_sel_hi:[0,1,1]
	v_pk_fma_f32 v[68:69], v[158:159], v[84:85], v[82:83] op_sel_hi:[0,1,1]
	v_mul_f32_e32 v168, 0.5, v72
	v_mul_f32_e32 v170, 0.5, v73
	s_waitcnt vmcnt(20)
	v_and_b32_e32 v73, 0xffff0000, v14
	v_lshlrev_b32_e32 v72, 16, v14
	v_and_b32_e32 v89, 0xffff0000, v15
	v_lshlrev_b32_e32 v88, 16, v15
	v_pk_fma_f32 v[66:67], v[160:161], v[70:71], v[66:67] op_sel_hi:[0,1,1]
	v_pk_fma_f32 v[68:69], v[160:161], v[86:87], v[68:69] op_sel_hi:[0,1,1]
	s_waitcnt vmcnt(19)
	v_and_b32_e32 v75, 0xffff0000, v18
	v_lshlrev_b32_e32 v74, 16, v18
	v_and_b32_e32 v177, 0xffff0000, v19
	v_lshlrev_b32_e32 v176, 16, v19
	v_pk_fma_f32 v[66:67], v[162:163], v[72:73], v[66:67] op_sel_hi:[0,1,1]
	v_pk_fma_f32 v[68:69], v[162:163], v[88:89], v[68:69] op_sel_hi:[0,1,1]
	s_waitcnt vmcnt(18)
	v_and_b32_e32 v77, 0xffff0000, v22
	v_lshlrev_b32_e32 v76, 16, v22
	v_and_b32_e32 v179, 0xffff0000, v23
	v_lshlrev_b32_e32 v178, 16, v23
	v_pk_fma_f32 v[66:67], v[164:165], v[74:75], v[66:67] op_sel_hi:[0,1,1]
	v_pk_fma_f32 v[68:69], v[164:165], v[176:177], v[68:69] op_sel_hi:[0,1,1]
	s_waitcnt vmcnt(17)
	v_and_b32_e32 v79, 0xffff0000, v26
	v_lshlrev_b32_e32 v78, 16, v26
	v_and_b32_e32 v181, 0xffff0000, v27
	v_lshlrev_b32_e32 v180, 16, v27
	v_pk_fma_f32 v[66:67], v[166:167], v[76:77], v[66:67] op_sel_hi:[0,1,1]
	v_pk_fma_f32 v[68:69], v[166:167], v[178:179], v[68:69] op_sel_hi:[0,1,1]
	s_waitcnt vmcnt(16)
	v_and_b32_e32 v81, 0xffff0000, v30
	v_lshlrev_b32_e32 v80, 16, v30
	v_and_b32_e32 v183, 0xffff0000, v31
	v_lshlrev_b32_e32 v182, 16, v31
	v_pk_fma_f32 v[66:67], v[168:169], v[78:79], v[66:67] op_sel_hi:[0,1,1]
	v_pk_fma_f32 v[68:69], v[168:169], v[180:181], v[68:69] op_sel_hi:[0,1,1]
	v_and_b32_e32 v99, 0xffff0000, v4
	v_lshlrev_b32_e32 v98, 16, v4
	v_pk_fma_f32 v[66:67], v[170:171], v[80:81], v[66:67] op_sel_hi:[0,1,1]
	v_pk_fma_f32 v[68:69], v[170:171], v[182:183], v[68:69] op_sel_hi:[0,1,1]
	v_cvt_pk_bf16_f32 v66, v66, v67
	v_cvt_pk_bf16_f32 v67, v68, v69
	v_pk_fma_f32 v[68:69], v[156:157], v[98:99], 0 op_sel_hi:[0,1,0]
	v_and_b32_e32 v71, 0xffff0000, v8
	v_lshlrev_b32_e32 v70, 16, v8
	v_pk_fma_f32 v[68:69], v[158:159], v[70:71], v[68:69] op_sel_hi:[0,1,1]
	v_and_b32_e32 v71, 0xffff0000, v12
	v_lshlrev_b32_e32 v70, 16, v12
	v_pk_fma_f32 v[68:69], v[160:161], v[70:71], v[68:69] op_sel_hi:[0,1,1]
	v_and_b32_e32 v71, 0xffff0000, v16
	v_lshlrev_b32_e32 v70, 16, v16
	v_pk_fma_f32 v[68:69], v[162:163], v[70:71], v[68:69] op_sel_hi:[0,1,1]
	v_and_b32_e32 v71, 0xffff0000, v20
	v_lshlrev_b32_e32 v70, 16, v20
	v_pk_fma_f32 v[68:69], v[164:165], v[70:71], v[68:69] op_sel_hi:[0,1,1]
	v_and_b32_e32 v71, 0xffff0000, v24
	v_lshlrev_b32_e32 v70, 16, v24
	v_pk_fma_f32 v[68:69], v[166:167], v[70:71], v[68:69] op_sel_hi:[0,1,1]
	v_and_b32_e32 v71, 0xffff0000, v28
	v_lshlrev_b32_e32 v70, 16, v28
	v_pk_fma_f32 v[68:69], v[168:169], v[70:71], v[68:69] op_sel_hi:[0,1,1]
	v_and_b32_e32 v71, 0xffff0000, v32
	v_lshlrev_b32_e32 v70, 16, v32
	v_pk_fma_f32 v[68:69], v[170:171], v[70:71], v[68:69] op_sel_hi:[0,1,1]
	v_and_b32_e32 v71, 0xffff0000, v5
	v_lshlrev_b32_e32 v70, 16, v5
	v_pk_fma_f32 v[70:71], v[156:157], v[70:71], 0 op_sel_hi:[0,1,0]
	v_and_b32_e32 v73, 0xffff0000, v9
	v_lshlrev_b32_e32 v72, 16, v9
	v_pk_fma_f32 v[70:71], v[158:159], v[72:73], v[70:71] op_sel_hi:[0,1,1]
	v_and_b32_e32 v73, 0xffff0000, v13
	v_lshlrev_b32_e32 v72, 16, v13
	v_pk_fma_f32 v[70:71], v[160:161], v[72:73], v[70:71] op_sel_hi:[0,1,1]
	v_and_b32_e32 v73, 0xffff0000, v17
	v_lshlrev_b32_e32 v72, 16, v17
	v_pk_fma_f32 v[70:71], v[162:163], v[72:73], v[70:71] op_sel_hi:[0,1,1]
	v_and_b32_e32 v73, 0xffff0000, v21
	v_lshlrev_b32_e32 v72, 16, v21
	v_pk_fma_f32 v[70:71], v[164:165], v[72:73], v[70:71] op_sel_hi:[0,1,1]
	v_and_b32_e32 v73, 0xffff0000, v25
	v_lshlrev_b32_e32 v72, 16, v25
	v_pk_fma_f32 v[70:71], v[166:167], v[72:73], v[70:71] op_sel_hi:[0,1,1]
	v_and_b32_e32 v73, 0xffff0000, v29
	v_lshlrev_b32_e32 v72, 16, v29
	v_pk_fma_f32 v[70:71], v[168:169], v[72:73], v[70:71] op_sel_hi:[0,1,1]
	v_and_b32_e32 v73, 0xffff0000, v33
	v_lshlrev_b32_e32 v72, 16, v33
	v_pk_fma_f32 v[70:71], v[170:171], v[72:73], v[70:71] op_sel_hi:[0,1,1]
	v_cvt_pk_bf16_f32 v68, v68, v69
	v_cvt_pk_bf16_f32 v69, v70, v71
	s_waitcnt vmcnt(15)
	v_and_b32_e32 v71, 0xffff0000, v34
	v_lshlrev_b32_e32 v70, 16, v34
	v_pk_fma_f32 v[70:71], v[156:157], v[70:71], 0 op_sel_hi:[0,1,0]
	s_waitcnt vmcnt(14)
	v_and_b32_e32 v73, 0xffff0000, v38
	v_lshlrev_b32_e32 v72, 16, v38
	v_pk_fma_f32 v[70:71], v[158:159], v[72:73], v[70:71] op_sel_hi:[0,1,1]
	s_waitcnt vmcnt(13)
	v_and_b32_e32 v73, 0xffff0000, v42
	v_lshlrev_b32_e32 v72, 16, v42
	v_pk_fma_f32 v[70:71], v[160:161], v[72:73], v[70:71] op_sel_hi:[0,1,1]
	s_waitcnt vmcnt(12)
	v_and_b32_e32 v73, 0xffff0000, v46
	v_lshlrev_b32_e32 v72, 16, v46
	v_pk_fma_f32 v[70:71], v[162:163], v[72:73], v[70:71] op_sel_hi:[0,1,1]
	s_waitcnt vmcnt(11)
	v_and_b32_e32 v73, 0xffff0000, v50
	v_lshlrev_b32_e32 v72, 16, v50
	v_pk_fma_f32 v[70:71], v[164:165], v[72:73], v[70:71] op_sel_hi:[0,1,1]
	s_waitcnt vmcnt(10)
	v_and_b32_e32 v73, 0xffff0000, v54
	v_lshlrev_b32_e32 v72, 16, v54
	v_pk_fma_f32 v[70:71], v[166:167], v[72:73], v[70:71] op_sel_hi:[0,1,1]
	s_waitcnt vmcnt(9)
	v_and_b32_e32 v73, 0xffff0000, v58
	v_lshlrev_b32_e32 v72, 16, v58
	v_pk_fma_f32 v[70:71], v[168:169], v[72:73], v[70:71] op_sel_hi:[0,1,1]
	s_waitcnt vmcnt(8)
	v_and_b32_e32 v73, 0xffff0000, v62
	v_lshlrev_b32_e32 v72, 16, v62
	v_pk_fma_f32 v[70:71], v[170:171], v[72:73], v[70:71] op_sel_hi:[0,1,1]
	v_and_b32_e32 v73, 0xffff0000, v35
	v_lshlrev_b32_e32 v72, 16, v35
	v_pk_fma_f32 v[72:73], v[156:157], v[72:73], 0 op_sel_hi:[0,1,0]
	v_and_b32_e32 v75, 0xffff0000, v39
	v_lshlrev_b32_e32 v74, 16, v39
	v_pk_fma_f32 v[72:73], v[158:159], v[74:75], v[72:73] op_sel_hi:[0,1,1]
	v_and_b32_e32 v75, 0xffff0000, v43
	v_lshlrev_b32_e32 v74, 16, v43
	v_pk_fma_f32 v[72:73], v[160:161], v[74:75], v[72:73] op_sel_hi:[0,1,1]
	v_and_b32_e32 v75, 0xffff0000, v47
	v_lshlrev_b32_e32 v74, 16, v47
	v_pk_fma_f32 v[72:73], v[162:163], v[74:75], v[72:73] op_sel_hi:[0,1,1]
	v_and_b32_e32 v75, 0xffff0000, v51
	v_lshlrev_b32_e32 v74, 16, v51
	v_pk_fma_f32 v[72:73], v[164:165], v[74:75], v[72:73] op_sel_hi:[0,1,1]
	v_and_b32_e32 v75, 0xffff0000, v55
	v_lshlrev_b32_e32 v74, 16, v55
	v_pk_fma_f32 v[72:73], v[166:167], v[74:75], v[72:73] op_sel_hi:[0,1,1]
	v_and_b32_e32 v75, 0xffff0000, v59
	v_lshlrev_b32_e32 v74, 16, v59
	v_pk_fma_f32 v[72:73], v[168:169], v[74:75], v[72:73] op_sel_hi:[0,1,1]
	v_and_b32_e32 v75, 0xffff0000, v63
	v_lshlrev_b32_e32 v74, 16, v63
	v_pk_fma_f32 v[72:73], v[170:171], v[74:75], v[72:73] op_sel_hi:[0,1,1]
	v_cvt_pk_bf16_f32 v70, v70, v71
	v_cvt_pk_bf16_f32 v71, v72, v73
	v_and_b32_e32 v73, 0xffff0000, v36
	v_lshlrev_b32_e32 v72, 16, v36
	v_pk_fma_f32 v[72:73], v[156:157], v[72:73], 0 op_sel_hi:[0,1,0]
	v_and_b32_e32 v75, 0xffff0000, v40
	v_lshlrev_b32_e32 v74, 16, v40
	v_pk_fma_f32 v[72:73], v[158:159], v[74:75], v[72:73] op_sel_hi:[0,1,1]
	v_and_b32_e32 v75, 0xffff0000, v44
	v_lshlrev_b32_e32 v74, 16, v44
	v_pk_fma_f32 v[72:73], v[160:161], v[74:75], v[72:73] op_sel_hi:[0,1,1]
	v_and_b32_e32 v75, 0xffff0000, v48
	v_lshlrev_b32_e32 v74, 16, v48
	v_pk_fma_f32 v[72:73], v[162:163], v[74:75], v[72:73] op_sel_hi:[0,1,1]
	v_and_b32_e32 v75, 0xffff0000, v52
	v_lshlrev_b32_e32 v74, 16, v52
	v_pk_fma_f32 v[72:73], v[164:165], v[74:75], v[72:73] op_sel_hi:[0,1,1]
	v_and_b32_e32 v75, 0xffff0000, v56
	v_lshlrev_b32_e32 v74, 16, v56
	v_pk_fma_f32 v[72:73], v[166:167], v[74:75], v[72:73] op_sel_hi:[0,1,1]
	v_and_b32_e32 v75, 0xffff0000, v60
	v_lshlrev_b32_e32 v74, 16, v60
	v_pk_fma_f32 v[72:73], v[168:169], v[74:75], v[72:73] op_sel_hi:[0,1,1]
	v_and_b32_e32 v75, 0xffff0000, v64
	v_lshlrev_b32_e32 v74, 16, v64
	v_pk_fma_f32 v[72:73], v[170:171], v[74:75], v[72:73] op_sel_hi:[0,1,1]
	v_and_b32_e32 v75, 0xffff0000, v37
	v_lshlrev_b32_e32 v74, 16, v37
	v_pk_fma_f32 v[74:75], v[156:157], v[74:75], 0 op_sel_hi:[0,1,0]
	v_and_b32_e32 v77, 0xffff0000, v41
	v_lshlrev_b32_e32 v76, 16, v41
	v_pk_fma_f32 v[74:75], v[158:159], v[76:77], v[74:75] op_sel_hi:[0,1,1]
	v_and_b32_e32 v77, 0xffff0000, v45
	v_lshlrev_b32_e32 v76, 16, v45
	v_pk_fma_f32 v[74:75], v[160:161], v[76:77], v[74:75] op_sel_hi:[0,1,1]
	v_and_b32_e32 v77, 0xffff0000, v49
	v_lshlrev_b32_e32 v76, 16, v49
	v_pk_fma_f32 v[74:75], v[162:163], v[76:77], v[74:75] op_sel_hi:[0,1,1]
	v_and_b32_e32 v77, 0xffff0000, v53
	v_lshlrev_b32_e32 v76, 16, v53
	v_pk_fma_f32 v[74:75], v[164:165], v[76:77], v[74:75] op_sel_hi:[0,1,1]
	v_and_b32_e32 v77, 0xffff0000, v57
	v_lshlrev_b32_e32 v76, 16, v57
	v_pk_fma_f32 v[74:75], v[166:167], v[76:77], v[74:75] op_sel_hi:[0,1,1]
	v_and_b32_e32 v77, 0xffff0000, v61
	v_lshlrev_b32_e32 v76, 16, v61
	v_pk_fma_f32 v[74:75], v[168:169], v[76:77], v[74:75] op_sel_hi:[0,1,1]
	v_and_b32_e32 v77, 0xffff0000, v65
	v_lshlrev_b32_e32 v76, 16, v65
	v_pk_fma_f32 v[74:75], v[170:171], v[76:77], v[74:75] op_sel_hi:[0,1,1]
	v_cvt_pk_bf16_f32 v72, v72, v73
	v_cvt_pk_bf16_f32 v73, v74, v75
	v_readlane_b32 s10, v254, 53
	s_waitcnt vmcnt(0)
	s_add_i32 s9, s10, s9
	s_min_i32 s9, s8, s9
	s_cmp_ge_i32 s12, s9
	s_cbranch_scc1 .LBB0_709
	v_readfirstlane_b32 s0, v138
	s_nop 3
	s_cmp_lt_u32 s0, 16
	s_cbranch_scc1 .Lstagger_skip
	s_sleep 55
	s_setprio 1

.LBB0_713:
	s_setprio 0
	v_readlane_b32 s0, v254, 56
	s_add_u32 s46, s0, s2
	v_readlane_b32 s0, v254, 57
	s_addc_u32 s47, s0, 0
	v_readlane_b32 s0, v254, 58
	s_add_u32 s48, s0, s2
	v_readlane_b32 s0, v254, 59
	s_addc_u32 s49, s0, 0
	s_lshl_b32 s52, s7, 4
	s_add_i32 s0, s52, 0xfffff100
	v_writelane_b32 v255, s0, 16
	s_add_i32 s0, s52, 0xfffff0c0
	v_writelane_b32 v255, s0, 17
	s_add_i32 s0, s52, 0xfffff080
	s_sub_i32 s26, s52, 64
	s_add_i32 s27, s52, 0xffffff80
	s_add_i32 s28, s52, 0xffffff40
	s_add_i32 s29, s52, 0xffffff00
	s_add_i32 s30, s52, 0xfffffec0
	s_add_i32 s31, s52, 0xfffffe80
	s_add_i32 s34, s52, 0xfffffe40
	s_add_i32 s35, s52, 0xfffffe00
	s_add_i32 s36, s52, 0xfffffdc0
	s_add_i32 s7, s52, 0xfffffd80
	s_add_i32 s37, s52, 0xfffffd40
	s_add_i32 s2, s52, 0xfffffd00
	s_add_i32 s38, s52, 0xfffffcc0
	s_add_i32 s39, s52, 0xfffffc80
	s_add_i32 s40, s52, 0xfffffc40
	s_add_i32 s41, s52, 0xfffffc00
	s_add_i32 s42, s52, 0xfffffbc0
	s_add_i32 s43, s52, 0xfffffb80
	s_add_i32 s33, s52, 0xfffffb40
	s_add_i32 s44, s52, 0xfffffb00
	s_add_i32 s45, s52, 0xfffffac0
	s_add_i32 s51, s52, 0xfffffa80
	s_add_i32 s50, s52, 0xfffffa40
	s_add_i32 s56, s52, 0xfffffa00
	s_add_i32 s55, s52, 0xfffff9c0
	s_add_i32 s58, s52, 0xfffff980
	s_add_i32 s57, s52, 0xfffff940
	s_add_i32 s63, s52, 0xfffff900
	s_add_i32 s59, s52, 0xfffff8c0
	s_add_i32 s62, s52, 0xfffff880
	s_add_i32 s65, s52, 0xfffff840
	s_add_i32 s64, s52, 0xfffff800
	s_add_i32 s67, s52, 0xfffff7c0
	s_add_i32 s66, s52, 0xfffff780
	s_add_i32 s68, s52, 0xfffff740
	s_add_i32 s69, s52, 0xfffff700
	s_add_i32 s70, s52, 0xfffff6c0
	s_add_i32 s72, s52, 0xfffff680
	s_add_i32 s71, s52, 0xfffff640
	s_add_i32 s73, s52, 0xfffff600
	s_add_i32 s74, s52, 0xfffff5c0
	s_add_i32 s75, s52, 0xfffff580
	s_add_i32 s76, s52, 0xfffff540
	s_add_i32 s77, s52, 0xfffff500
	s_add_i32 s78, s52, 0xfffff4c0
	s_add_i32 s79, s52, 0xfffff480
	s_add_i32 s96, s52, 0xfffff440
	s_add_i32 s82, s52, 0xfffff400
	s_add_i32 s83, s52, 0xfffff3c0
	s_add_i32 s84, s52, 0xfffff380
	s_add_i32 s85, s52, 0xfffff340
	s_add_i32 s86, s52, 0xfffff300
	s_add_i32 s87, s52, 0xfffff2c0
	s_add_i32 s88, s52, 0xfffff280
	s_add_i32 s89, s52, 0xfffff240
	s_add_i32 s90, s52, 0xfffff200
	s_add_i32 s91, s52, 0xfffff1c0
	s_add_i32 s92, s52, 0xfffff180
	s_add_i32 s94, s52, 0xfffff140
	v_writelane_b32 v255, s0, 18
	s_add_i32 s0, s52, 0xfffff040
	s_cmpk_gt_i32 s6, 0xffe0
	s_cselect_b64 s[60:61], -1, 0
	s_cmpk_gt_i32 s6, 0x3ff
	v_writelane_b32 v255, s0, 19
	s_cselect_b64 s[0:1], -1, 0
	v_writelane_b32 v255, s0, 20
	s_cmpk_gt_i32 s6, 0x7ff
	s_nop 0
	v_writelane_b32 v255, s1, 21
	s_cselect_b64 s[0:1], -1, 0
	v_writelane_b32 v255, s0, 22
	s_cmpk_gt_i32 s6, 0xbff
	s_barrier
	v_writelane_b32 v255, s1, 23
	s_cselect_b64 s[0:1], -1, 0
	v_writelane_b32 v255, s0, 24
	s_cmpk_gt_i32 s6, 0xfff
	s_nop 0
	v_writelane_b32 v255, s1, 25
	s_cselect_b64 s[0:1], -1, 0
	v_writelane_b32 v255, s0, 26
	s_cmpk_gt_i32 s6, 0x13ff
	s_nop 0
	v_writelane_b32 v255, s1, 27
	s_cselect_b64 s[0:1], -1, 0
	v_writelane_b32 v255, s0, 28
	s_cmpk_gt_i32 s6, 0x17ff
	s_nop 0
	v_writelane_b32 v255, s1, 29
	s_cselect_b64 s[0:1], -1, 0
	v_writelane_b32 v255, s0, 30
	s_cmpk_gt_i32 s6, 0x1bff
	s_nop 0
	v_writelane_b32 v255, s1, 31
	s_cselect_b64 s[0:1], -1, 0
	v_writelane_b32 v255, s0, 32
	s_nop 1
	v_writelane_b32 v255, s1, 33
	v_writelane_b32 v255, s69, 34
	v_writelane_b32 v255, s46, 35
	s_nop 1
	v_writelane_b32 v255, s47, 36
	v_writelane_b32 v255, s71, 37
	v_writelane_b32 v255, s73, 38
	v_writelane_b32 v255, s64, 39
	v_writelane_b32 v255, s75, 40
	v_writelane_b32 v255, s66, 41
	v_writelane_b32 v255, s77, 42
	v_writelane_b32 v255, s68, 43
	v_writelane_b32 v255, s79, 44
	v_writelane_b32 v255, s44, 45
	v_writelane_b32 v255, s82, 46
	v_writelane_b32 v255, s83, 47
	v_writelane_b32 v255, s84, 48
	v_writelane_b32 v255, s85, 49
	v_writelane_b32 v255, s86, 50
	v_writelane_b32 v255, s87, 51
	v_writelane_b32 v255, s88, 52
	v_writelane_b32 v255, s89, 53
	v_writelane_b32 v255, s90, 54
	v_writelane_b32 v255, s91, 55
	v_writelane_b32 v255, s92, 56
	v_writelane_b32 v255, s94, 57
	s_branch .LBB0_716
